# baseline (speedup 1.0000x reference)
_Z11gram_kernelPKfPKiS0_S0_S0_S0_S0_S0_S0_S0_S0_Pf:
	s_load_dwordx4 s[24:27], s[0:1], 0x0
	s_load_dwordx2 s[28:29], s[0:1], 0x40
	s_load_dwordx4 s[20:23], s[0:1], 0x30
	s_load_dwordx2 s[10:11], s[0:1], 0x58
	s_load_dwordx2 s[44:45], s[0:1], 0x20
	s_load_dwordx2 s[68:69], s[0:1], 0x10
	s_load_dwordx2 s[60:61], s[0:1], 0x18
	s_load_dwordx2 s[62:63], s[0:1], 0x28
	s_load_dwordx2 s[64:65], s[0:1], 0x48
	s_load_dwordx2 s[66:67], s[0:1], 0x50
	s_ashr_i32 s30, s2, 1
	v_mov_b32_e32 v11, 0
	s_ashr_i32 s31, s30, 31
	s_lshl_b32 s46, s30, 11
	s_lshl_b32 s3, s2, 10
	s_ashr_i32 s47, s46, 31
	s_and_b32 s33, s3, 0x400
	v_lshlrev_b32_e32 v46, 2, v0
	v_mov_b32_e32 v47, 0
	v_lshlrev_b32_e32 v212, 1, v0
	v_mov_b32_e32 v213, v47
	v_lshrrev_b32_e32 v219, 6, v0
	v_bfe_u32 v214, v0, 5, 1
	v_and_b32_e32 v220, 31, v0
	s_or_b32 s3, s46, s33
	v_lshlrev_b32_e32 v216, 4, v219
	v_lshlrev_b32_e32 v221, 3, v214
	v_or3_b32 v1, s3, v216, v221
	v_lshlrev_b32_e32 v232, 4, v220
	v_and_b32_e32 v218, 63, v0
	s_mov_b32 s39, 0x20000
	s_brev_b32 s38, 16
	v_lshl_or_b32 v180, v1, 9, v232
	v_add_u32_e32 v1, 0x10000, v180
	s_lshl_b64 s[4:5], s[46:47], 2
	s_lshl_b32 s3, s33, 2
	v_lshlrev_b32_e32 v251, 7, v0
	v_and_b32_e32 v252, 0x3fff, v251
	v_and_b32_e32 v253, 0x1fc, v46
	s_lshl_b64 s[6:7], s[30:31], 14
	s_waitcnt lgkmcnt(0)
	s_add_u32 s48, s20, s6
	s_addc_u32 s49, s21, s7
	s_mov_b64 s[36:37], s[24:25]
	s_and_b32 s37, s37, 0xffff
	s_add_u32 s26, s26, s4
	s_addc_u32 s27, s27, s5
	s_add_u32 s26, s26, s3
	s_addc_u32 s27, s27, 0
	v_lshl_add_u64 v[32:33], v[212:213], 2, s[26:27]
	global_load_dwordx2 v[32:33], v[32:33], off
	buffer_load_dwordx4 v[34:37], v180, s[36:39], 0 offen nt
	buffer_load_dwordx4 v[38:41], v180, s[36:39], 0 offen offset:512 nt
	buffer_load_dwordx4 v[42:45], v180, s[36:39], 0 offen offset:1024 nt
	buffer_load_dwordx4 v[96:99], v180, s[36:39], 0 offen offset:1536 nt
	buffer_load_dwordx4 v[100:103], v180, s[36:39], 0 offen offset:2048 nt
	buffer_load_dwordx4 v[104:107], v180, s[36:39], 0 offen offset:2560 nt
	buffer_load_dwordx4 v[108:111], v180, s[36:39], 0 offen offset:3072 nt
	buffer_load_dwordx4 v[112:115], v180, s[36:39], 0 offen offset:3584 nt
	global_load_dword v250, v251, s[22:23]
	global_load_dword v250, v251, s[28:29]
	global_load_dword v250, v251, s[68:69]
	global_load_dword v250, v251, s[44:45]
	global_load_dword v250, v252, s[48:49]
	global_load_dword v250, v253, s[60:61]
	global_load_dword v250, v253, s[62:63]
	global_load_dword v250, v253, s[64:65]
	global_load_dword v250, v47, s[66:67]
	buffer_load_dwordx4 v[116:119], v1, s[36:39], 0 offen nt
	buffer_load_dwordx4 v[120:123], v1, s[36:39], 0 offen offset:512 nt
	buffer_load_dwordx4 v[124:127], v1, s[36:39], 0 offen offset:1024 nt
	buffer_load_dwordx4 v[128:131], v1, s[36:39], 0 offen offset:1536 nt
	buffer_load_dwordx4 v[132:135], v1, s[36:39], 0 offen offset:2048 nt
	buffer_load_dwordx4 v[136:139], v1, s[36:39], 0 offen offset:2560 nt
	buffer_load_dwordx4 v[140:143], v1, s[36:39], 0 offen offset:3072 nt
	buffer_load_dwordx4 v[144:147], v1, s[36:39], 0 offen offset:3584 nt
	s_movk_i32 s3, 0x160
	v_cmp_gt_u32_e32 vcc, s3, v0
	s_mov_b32 s3, 0x10000
	v_lshrrev_b32_e32 v227, 5, v0
	v_and_b32_e32 v228, 0x7c, v46
	v_add_u32_e32 v2, 0x200, v0
	v_lshrrev_b32_e32 v229, 5, v2
	v_mul_u32_u24_e32 v246, 0x110, v227
	v_lshl_add_u32 v246, v220, 3, v246
	v_add_u32_e32 v246, 0x10000, v246
	v_lshlrev_b32_e32 v247, 2, v46
	s_waitcnt vmcnt(25)
	v_cmp_ne_u32_e64 s[6:7], 0, v32
	v_cmp_ne_u32_e64 s[4:5], 0, v33
	v_cmp_eq_u32_e64 s[8:9], 0, v218
	s_nop 0
	s_and_saveexec_b64 s[12:13], s[8:9]
	s_cbranch_execz .LBB0_6
	s_bcnt1_i32_b64 s6, s[6:7]
	s_bcnt1_i32_b64 s4, s[4:5]
	v_mov_b32_e32 v1, 0x21100
	s_add_i32 s4, s4, s6
	v_lshl_add_u32 v1, v219, 2, v1
	v_mov_b32_e32 v2, s4
	ds_write_b32 v1, v2

	.amdhsa_kernel _Z11gram_kernelPKfPKiS0_S0_S0_S0_S0_S0_S0_S0_S0_Pf
		.amdhsa_group_segment_fixed_size 135456
		.amdhsa_private_segment_fixed_size 0
		.amdhsa_kernarg_size 96
		.amdhsa_user_sgpr_count 2
		.amdhsa_user_sgpr_dispatch_ptr 0
		.amdhsa_user_sgpr_queue_ptr 0
		.amdhsa_user_sgpr_kernarg_segment_ptr 1
		.amdhsa_user_sgpr_dispatch_id 0
		.amdhsa_user_sgpr_kernarg_preload_length 0
		.amdhsa_user_sgpr_kernarg_preload_offset 0
		.amdhsa_user_sgpr_private_segment_size 0
		.amdhsa_uses_dynamic_stack 0
		.amdhsa_enable_private_segment 0
		.amdhsa_system_sgpr_workgroup_id_x 1
		.amdhsa_system_sgpr_workgroup_id_y 0
		.amdhsa_system_sgpr_workgroup_id_z 0
		.amdhsa_system_sgpr_workgroup_info 0
		.amdhsa_system_vgpr_workitem_id 0
		.amdhsa_next_free_vgpr 254
		.amdhsa_next_free_sgpr 96
		.amdhsa_accum_offset 256
		.amdhsa_reserve_vcc 1
		.amdhsa_float_round_mode_32 0
		.amdhsa_float_round_mode_16_64 0
		.amdhsa_float_denorm_mode_32 3
		.amdhsa_float_denorm_mode_16_64 3
		.amdhsa_dx10_clamp 1
		.amdhsa_ieee_mode 1
		.amdhsa_fp16_overflow 0
		.amdhsa_tg_split 0
		.amdhsa_exception_fp_ieee_invalid_op 0
		.amdhsa_exception_fp_denorm_src 0
		.amdhsa_exception_fp_ieee_div_zero 0
		.amdhsa_exception_fp_ieee_overflow 0
		.amdhsa_exception_fp_ieee_underflow 0
		.amdhsa_exception_fp_ieee_inexact 0
		.amdhsa_exception_int_div_zero 0
	.end_amdhsa_kernel

amdhsa.kernels:
  - .agpr_count:     0
    .args:
      - .actual_access:  read_only
        .address_space:  global
        .offset:         0
        .size:           8
        .value_kind:     global_buffer
      - .actual_access:  read_only
        .address_space:  global
        .offset:         8
        .size:           8
        .value_kind:     global_buffer
      - .actual_access:  read_only
        .address_space:  global
        .offset:         16
        .size:           8
        .value_kind:     global_buffer
      - .actual_access:  read_only
        .address_space:  global
        .offset:         24
        .size:           8
        .value_kind:     global_buffer
      - .actual_access:  read_only
        .address_space:  global
        .offset:         32
        .size:           8
        .value_kind:     global_buffer
      - .actual_access:  read_only
        .address_space:  global
        .offset:         40
        .size:           8
        .value_kind:     global_buffer
      - .address_space:  global
        .offset:         48
        .size:           8
        .value_kind:     global_buffer
      - .address_space:  global
        .offset:         56
        .size:           8
        .value_kind:     global_buffer
      - .address_space:  global
        .offset:         64
        .size:           8
        .value_kind:     global_buffer
      - .actual_access:  read_only
        .address_space:  global
        .offset:         72
        .size:           8
        .value_kind:     global_buffer
      - .actual_access:  read_only
        .address_space:  global
        .offset:         80
        .size:           8
        .value_kind:     global_buffer
      - .actual_access:  write_only
        .address_space:  global
        .offset:         88
        .size:           8
        .value_kind:     global_buffer
    .group_segment_fixed_size: 135456
    .kernarg_segment_align: 8
    .kernarg_segment_size: 96
    .language:       OpenCL C
    .language_version:
      - 2
      - 0
    .max_flat_workgroup_size: 512
    .name:           _Z11gram_kernelPKfPKiS0_S0_S0_S0_S0_S0_S0_S0_S0_Pf
    .private_segment_fixed_size: 0
    .sgpr_count:     66
    .sgpr_spill_count: 0
    .symbol:         _Z11gram_kernelPKfPKiS0_S0_S0_S0_S0_S0_S0_S0_S0_Pf.kd
    .uniform_work_group_size: 1
    .uses_dynamic_stack: false
    .vgpr_count:     254
    .vgpr_spill_count: 0
    .wavefront_size: 64
  - .agpr_count:     0
    .args:
      - .actual_access:  read_only
        .address_space:  global
        .offset:         0
        .size:           8
        .value_kind:     global_buffer
      - .actual_access:  read_only
        .address_space:  global
        .offset:         8
        .size:           8
        .value_kind:     global_buffer
      - .actual_access:  write_only
        .address_space:  global
        .offset:         16
        .size:           8
        .value_kind:     global_buffer
    .group_segment_fixed_size: 0
    .kernarg_segment_align: 8
    .kernarg_segment_size: 24
    .language:       OpenCL C
    .language_version:
      - 2
      - 0
    .max_flat_workgroup_size: 256
    .name:           _Z10fin_kernelPKfS0_Pf
    .private_segment_fixed_size: 0
    .sgpr_count:     16
    .sgpr_spill_count: 0
    .symbol:         _Z10fin_kernelPKfS0_Pf.kd
    .uniform_work_group_size: 1
    .uses_dynamic_stack: false
    .vgpr_count:     51
    .vgpr_spill_count: 0
    .wavefront_size: 64
